# Deferred layer-1 MoE weight conversion now consumed at five idle points (ends of out-proj L0, top-k L0, in-proj L1, NA/GLA, out-proj L1: workgroups convert until all 256 have arrived), final drain by
# baseline (speedup 1.0000x reference)
; #define LAS __attribute__((address_space(3)))
; __device__ __forceinline__ void lds_barrier() { asm volatile("s_waitcnt lgkmcnt(0)" ::: "memory"); __builtin_amdgcn_s_barrier(); asm volatile("" ::: "memory"); }
; __device__ __forceinline__ unsigned xb_add(unsigned* p, unsigned v) { return __hip_atomic_fetch_add(p, v, __ATOMIC_RELAXED, __HIP_MEMORY_SCOPE_AGENT); }
; __device__ __forceinline__ void phase_prologue(const Args& a, LAS unsigned char* lds) {
;     ...
;     unsigned* cq_head = (unsigned*)(a.ws + WS_CTL) + 8192 + 768;
;     volatile LAS int* qs = (volatile LAS int*)(lds + 128 * 129 * 4);
;     int pend = 0, it = 0;
;     if (tid == 0) { qs[0] = (int)xb_add(cq_head, 1u); pend = (int)xb_add(cq_head, 1u); }
;     __syncthreads();
;     for (int u = qs[0]; u < CTOT; u = qs[it & 1]) {
;     ...
;         ++it;
;         if (tid == 0) { qs[it & 1] = pend; pend = (int)xb_add(cq_head, 1u); }
;         lds_barrier();
.LBB0_560:
.Lcvc_entry:
	s_waitcnt vmcnt(0) lgkmcnt(0)
	s_barrier
	v_mov_b32_e32 v119, 1
	v_mov_b32_e32 v120, 0x9000
	v_mov_b32_e32 v121, 0x9180
	v_mov_b32_e32 v122, 0
	v_mov_b32_e32 v125, 0x10200
	s_mov_b32 s67, 0
	v_cmp_eq_u32_e32 vcc, 0, v0
	s_and_saveexec_b64 s[76:77], vcc
	s_cbranch_execz .Lcvc_f0
	global_atomic_add v124, v121, v119, s[94:95] sc0
	s_waitcnt vmcnt(0)
	v_add_u32_e32 v124, 1, v124
	ds_write_b32 v125, v124 offset:4
.Lcvc_f0:
	s_mov_b64 exec, s[76:77]
	s_waitcnt lgkmcnt(0)
	s_barrier
	ds_read_b32 v127, v125 offset:4
	s_waitcnt lgkmcnt(0)
	v_readfirstlane_b32 s67, v127
	s_cmpk_ge_u32 s67, 0x100
	s_cbranch_scc1 .Lcvc_done
	s_barrier
	v_lshrrev_b32_e32 v104, 5, v0
	v_and_b32_e32 v126, 31, v0
	v_lshlrev_b32_e32 v105, 13, v104
	v_lshl_add_u32 v105, v126, 4, v105
	v_add_u32_e32 v106, 0x20000, v105
	v_add_u32_e32 v107, 0x40000, v105
	v_add_u32_e32 v108, 0x60000, v105
	v_add_u32_e32 v109, 0x80000, v105
	v_add_u32_e32 v110, 0xa0000, v105
	v_add_u32_e32 v111, 0xc0000, v105
	v_add_u32_e32 v112, 0xe0000, v105
	v_mul_u32_u24_e32 v113, 0x204, v104
	v_lshl_add_u32 v113, v126, 4, v113
	v_lshrrev_b32_e32 v127, 4, v0
	v_and_b32_e32 v126, 15, v0
	v_mul_u32_u24_e32 v114, 0x1020, v126
	v_lshl_add_u32 v114, v127, 2, v114
	v_lshlrev_b32_e32 v115, 12, v127
	v_lshl_add_u32 v115, v126, 4, v115
	v_add_u32_e32 v116, 0x20000, v115
	v_add_u32_e32 v117, 0x40000, v115
	v_add_u32_e32 v118, 0x60000, v115
	v_readlane_b32 s82, v254, 27
	v_readlane_b32 s83, v254, 28
	s_sub_u32 s82, s82, 0x28
	s_subb_u32 s83, s83, 0
	s_load_dwordx2 s[80:81], s[82:83], 0x0
	s_waitcnt lgkmcnt(0)
	v_cmp_eq_u32_e32 vcc, 0, v0
	s_and_saveexec_b64 s[76:77], vcc
	s_cbranch_execz .Lcvc_t0a
	global_atomic_add v123, v120, v119, s[94:95] sc0
	s_waitcnt vmcnt(0)
	ds_write_b32 v125, v123
	ds_write_b32 v125, v122 offset:4
.Lcvc_t0a:
	s_mov_b64 exec, s[76:77]
	s_waitcnt lgkmcnt(0)
	s_barrier
.Lcvc_loop:
	ds_read_b32 v126, v125
	ds_read_b32 v127, v125 offset:4
	s_waitcnt lgkmcnt(0)
	v_readfirstlane_b32 s66, v126
	v_readfirstlane_b32 s67, v127
	s_cmpk_gt_u32 s66, 0x1fff
	s_cbranch_scc1 .Lcvc_done
	s_cmpk_ge_u32 s67, 0x100
	s_cbranch_scc1 .Lcvc_nopf
	v_cmp_eq_u32_e32 vcc, 0, v0
	s_and_saveexec_b64 s[76:77], vcc
	s_cbranch_execz .Lcvc_t0b
	global_atomic_add v123, v120, v119, s[94:95] sc0
	global_atomic_add v124, v121, v122, s[94:95] sc0
.Lcvc_t0b:
	s_mov_b64 exec, s[76:77]
; #define LAS __attribute__((address_space(3)))
; __device__ __forceinline__ void lds_barrier() { asm volatile("s_waitcnt lgkmcnt(0)" ::: "memory"); __builtin_amdgcn_s_barrier(); asm volatile("" ::: "memory"); }
; __device__ __forceinline__ unsigned xb_add(unsigned* p, unsigned v) { return __hip_atomic_fetch_add(p, v, __ATOMIC_RELAXED, __HIP_MEMORY_SCOPE_AGENT); }
; __device__ __forceinline__ void phase_prologue(const Args& a, LAS unsigned char* lds) {
;     ...
;         const int kt = r / NT, ntl = r % NT, k0 = kt * 128, n0 = ntl * 128;
;         const int drow0 = mode == 0 ? n0 : (ntl * 256 + (mode == 2 ? 128 : 0));
;         f32x4 v[8];
; #pragma unroll
;         for (int i = 0; i < 8; ++i) { const int id = tid + 512 * i, row = id >> 5, c4 = id & 31, n = n0 + c4 * 4;
;             v[i] = (f32x4){0.f, 0.f, 0.f, 0.f};
;             if (n < nvalid) v[i] = *(const f32x4*)(src + (size_t)(k0 + row) * ldn + n); }
; #pragma unroll
;         for (int i = 0; i < 8; ++i) { const int id = tid + 512 * i, row = id >> 5, c4 = id & 31;
;             LAS float* tp = tile + row * 129 + c4 * 4; tp[0] = v[i][0]; tp[1] = v[i][1]; tp[2] = v[i][2]; tp[3] = v[i][3]; }
;         lds_barrier();
; #pragma unroll
;         for (int i = 0; i < 4; ++i) { const int piece = tid + 512 * i, nl = piece >> 4, kg = piece & 15; const LAS float* s = tile + (kg * 8) * 129 + nl;
;             u32x4 o; o.x = pk2(s[0], s[129]); o.y = pk2(s[258], s[387]); o.z = pk2(s[516], s[645]); o.w = pk2(s[774], s[903]);
;             *(u32x4*)(dst + (size_t)(drow0 + nl) * 2048 + k0 + kg * 8) = o; }
;         ++it;
;         if (tid == 0) { qs[it & 1] = pend; pend = (int)xb_add(cq_head, 1u); }
;         lds_barrier();
.Lcvc_nopf:
	s_lshr_b32 s78, s66, 12
	s_bfe_u32 s72, s66, 0x40008
	s_add_i32 s72, s72, 16
	s_lshl_b32 s72, s72, 24
	s_bfe_u32 s73, s66, 0x40004
	s_and_b32 s74, s66, 15
	v_readlane_b32 s68, v254, 43
	v_readlane_b32 s69, v254, 44
	s_cmp_lg_u32 s78, 0
	s_cselect_b32 s68, s80, s68
	s_cselect_b32 s69, s81, s69
	s_lshl_b32 s75, s73, 20
	s_add_i32 s75, s75, s72
	s_lshl_b32 s79, s74, 9
	s_add_i32 s75, s75, s79
	s_add_u32 s68, s68, s75
	s_addc_u32 s69, s69, 0
	v_readlane_b32 s70, v254, 25
	v_readlane_b32 s71, v254, 26
	s_lshl_b32 s75, s74, 20
	s_add_i32 s75, s75, s72
	s_lshl_b32 s79, s78, 19
	s_add_i32 s75, s75, s79
	s_lshl_b32 s79, s73, 8
	s_add_i32 s75, s75, s79
	s_add_u32 s70, s70, s75
	s_addc_u32 s71, s71, 0
	global_load_dwordx4 v[128:131], v105, s[68:69]
	global_load_dwordx4 v[132:135], v106, s[68:69]
	global_load_dwordx4 v[136:139], v107, s[68:69]
	global_load_dwordx4 v[140:143], v108, s[68:69]
	global_load_dwordx4 v[144:147], v109, s[68:69]
	global_load_dwordx4 v[148:151], v110, s[68:69]
	global_load_dwordx4 v[152:155], v111, s[68:69]
	global_load_dwordx4 v[156:159], v112, s[68:69]
	s_waitcnt vmcnt(7)
	ds_write_b32 v113, v128
	ds_write_b32 v113, v129 offset:4
	ds_write_b32 v113, v130 offset:8
	ds_write_b32 v113, v131 offset:12
	s_waitcnt vmcnt(6)
	ds_write_b32 v113, v132 offset:8256
	ds_write_b32 v113, v133 offset:8260
	ds_write_b32 v113, v134 offset:8264
	ds_write_b32 v113, v135 offset:8268
	s_waitcnt vmcnt(5)
	ds_write_b32 v113, v136 offset:16512
	ds_write_b32 v113, v137 offset:16516
	ds_write_b32 v113, v138 offset:16520
	ds_write_b32 v113, v139 offset:16524
	s_waitcnt vmcnt(4)
	ds_write_b32 v113, v140 offset:24768
	ds_write_b32 v113, v141 offset:24772
	ds_write_b32 v113, v142 offset:24776
	ds_write_b32 v113, v143 offset:24780
	s_waitcnt vmcnt(3)
	ds_write_b32 v113, v144 offset:33024
	ds_write_b32 v113, v145 offset:33028
	ds_write_b32 v113, v146 offset:33032
	ds_write_b32 v113, v147 offset:33036
	s_waitcnt vmcnt(2)
	ds_write_b32 v113, v148 offset:41280
	ds_write_b32 v113, v149 offset:41284
	ds_write_b32 v113, v150 offset:41288
	ds_write_b32 v113, v151 offset:41292
	s_waitcnt vmcnt(1)
	ds_write_b32 v113, v152 offset:49536
	ds_write_b32 v113, v153 offset:49540
	ds_write_b32 v113, v154 offset:49544
	ds_write_b32 v113, v155 offset:49548
	s_waitcnt vmcnt(0)
	ds_write_b32 v113, v156 offset:57792
	ds_write_b32 v113, v157 offset:57796
	ds_write_b32 v113, v158 offset:57800
	ds_write_b32 v113, v159 offset:57804
	s_waitcnt lgkmcnt(0)
	s_barrier
	ds_read_b32 v160, v114
	ds_read_b32 v161, v114 offset:516
	ds_read_b32 v162, v114 offset:1032
	ds_read_b32 v163, v114 offset:1548
	ds_read_b32 v164, v114 offset:2064
	ds_read_b32 v165, v114 offset:2580
	ds_read_b32 v166, v114 offset:3096
	ds_read_b32 v167, v114 offset:3612
	s_waitcnt lgkmcnt(0)
	v_cvt_pk_bf16_f32 v168, v160, v161
	v_cvt_pk_bf16_f32 v169, v162, v163
	v_cvt_pk_bf16_f32 v170, v164, v165
	v_cvt_pk_bf16_f32 v171, v166, v167
	global_store_dwordx4 v115, v[168:171], s[70:71]
	ds_read_b32 v160, v114 offset:128
	ds_read_b32 v161, v114 offset:644
	ds_read_b32 v162, v114 offset:1160
	ds_read_b32 v163, v114 offset:1676
	ds_read_b32 v164, v114 offset:2192
	ds_read_b32 v165, v114 offset:2708
	ds_read_b32 v166, v114 offset:3224
	ds_read_b32 v167, v114 offset:3740
	s_waitcnt lgkmcnt(0)
	v_cvt_pk_bf16_f32 v172, v160, v161
	v_cvt_pk_bf16_f32 v173, v162, v163
	v_cvt_pk_bf16_f32 v174, v164, v165
	v_cvt_pk_bf16_f32 v175, v166, v167
	global_store_dwordx4 v116, v[172:175], s[70:71]
	ds_read_b32 v160, v114 offset:256
	ds_read_b32 v161, v114 offset:772
	ds_read_b32 v162, v114 offset:1288
	ds_read_b32 v163, v114 offset:1804
	ds_read_b32 v164, v114 offset:2320
	ds_read_b32 v165, v114 offset:2836
	ds_read_b32 v166, v114 offset:3352
	ds_read_b32 v167, v114 offset:3868
	s_waitcnt lgkmcnt(0)
	v_cvt_pk_bf16_f32 v168, v160, v161
	v_cvt_pk_bf16_f32 v169, v162, v163
	v_cvt_pk_bf16_f32 v170, v164, v165
	v_cvt_pk_bf16_f32 v171, v166, v167
	global_store_dwordx4 v117, v[168:171], s[70:71]
	ds_read_b32 v160, v114 offset:384
	ds_read_b32 v161, v114 offset:900
	ds_read_b32 v162, v114 offset:1416
	ds_read_b32 v163, v114 offset:1932
	ds_read_b32 v164, v114 offset:2448
	ds_read_b32 v165, v114 offset:2964
	ds_read_b32 v166, v114 offset:3480
	ds_read_b32 v167, v114 offset:3996
	s_waitcnt lgkmcnt(0)
	v_cvt_pk_bf16_f32 v172, v160, v161
	v_cvt_pk_bf16_f32 v173, v162, v163
	v_cvt_pk_bf16_f32 v174, v164, v165
	v_cvt_pk_bf16_f32 v175, v166, v167
	global_store_dwordx4 v118, v[172:175], s[70:71]
	s_cmpk_ge_u32 s67, 0x100
	s_cbranch_scc1 .Lcvc_done
	v_cmp_eq_u32_e32 vcc, 0, v0
	s_and_saveexec_b64 s[76:77], vcc
	s_cbranch_execz .Lcvc_t0c
	s_waitcnt vmcnt(0)
	ds_write_b32 v125, v123
	ds_write_b32 v125, v124 offset:4
.Lcvc_t0c:
	s_mov_b64 exec, s[76:77]
	s_waitcnt lgkmcnt(0)
	s_barrier
	s_branch .Lcvc_loop

; #define LAS __attribute__((address_space(3)))
; __device__ __forceinline__ unsigned xb_add(unsigned* p, unsigned v) { return __hip_atomic_fetch_add(p, v, __ATOMIC_RELAXED, __HIP_MEMORY_SCOPE_AGENT); }
; __device__ __forceinline__ void phase_prologue(const Args& a, LAS unsigned char* lds) {
;     ...
;     unsigned* cq_head = (unsigned*)(a.ws + WS_CTL) + 8192 + 768;
;     volatile LAS int* qs = (volatile LAS int*)(lds + 128 * 129 * 4);
;     int pend = 0, it = 0;
;     if (tid == 0) { qs[0] = (int)xb_add(cq_head, 1u); pend = (int)xb_add(cq_head, 1u); }
;     __syncthreads();
.LBB0_768:
.Lcvd_entry:
	s_waitcnt vmcnt(0) lgkmcnt(0)
	s_barrier
	v_mov_b32_e32 v119, 1
	v_mov_b32_e32 v120, 0x9000
	v_mov_b32_e32 v121, 0x9200
	v_mov_b32_e32 v122, 0
	v_mov_b32_e32 v125, 0x10200
	s_mov_b32 s67, 0
	v_cmp_eq_u32_e32 vcc, 0, v0
	s_and_saveexec_b64 s[76:77], vcc
	s_cbranch_execz .Lcvd_f0
	global_atomic_add v124, v121, v119, s[94:95] sc0
	s_waitcnt vmcnt(0)
	v_add_u32_e32 v124, 1, v124
	ds_write_b32 v125, v124 offset:4

; #define LAS __attribute__((address_space(3)))
; __device__ __forceinline__ void lds_barrier() { asm volatile("s_waitcnt lgkmcnt(0)" ::: "memory"); __builtin_amdgcn_s_barrier(); asm volatile("" ::: "memory"); }
; __device__ __forceinline__ unsigned xb_add(unsigned* p, unsigned v) { return __hip_atomic_fetch_add(p, v, __ATOMIC_RELAXED, __HIP_MEMORY_SCOPE_AGENT); }
; __device__ __forceinline__ void phase_prologue(const Args& a, LAS unsigned char* lds) {
;     ...
;     unsigned* cq_head = (unsigned*)(a.ws + WS_CTL) + 8192 + 768;
;     volatile LAS int* qs = (volatile LAS int*)(lds + 128 * 129 * 4);
;     int pend = 0, it = 0;
;     if (tid == 0) { qs[0] = (int)xb_add(cq_head, 1u); pend = (int)xb_add(cq_head, 1u); }
;     __syncthreads();
;     for (int u = qs[0]; u < CTOT; u = qs[it & 1]) {
;     ...
;         const int kt = r / NT, ntl = r % NT, k0 = kt * 128, n0 = ntl * 128;
;         const int drow0 = mode == 0 ? n0 : (ntl * 256 + (mode == 2 ? 128 : 0));
;         f32x4 v[8];
; #pragma unroll
;         for (int i = 0; i < 8; ++i) { const int id = tid + 512 * i, row = id >> 5, c4 = id & 31, n = n0 + c4 * 4;
;             v[i] = (f32x4){0.f, 0.f, 0.f, 0.f};
;             if (n < nvalid) v[i] = *(const f32x4*)(src + (size_t)(k0 + row) * ldn + n); }
; #pragma unroll
;         for (int i = 0; i < 8; ++i) { const int id = tid + 512 * i, row = id >> 5, c4 = id & 31;
;             LAS float* tp = tile + row * 129 + c4 * 4; tp[0] = v[i][0]; tp[1] = v[i][1]; tp[2] = v[i][2]; tp[3] = v[i][3]; }
;         lds_barrier();
; #pragma unroll
;         for (int i = 0; i < 4; ++i) { const int piece = tid + 512 * i, nl = piece >> 4, kg = piece & 15; const LAS float* s = tile + (kg * 8) * 129 + nl;
;             u32x4 o; o.x = pk2(s[0], s[129]); o.y = pk2(s[258], s[387]); o.z = pk2(s[516], s[645]); o.w = pk2(s[774], s[903]);
;             *(u32x4*)(dst + (size_t)(drow0 + nl) * 2048 + k0 + kg * 8) = o; }
.LBB0_1079:
.Lcve_entry:
	s_waitcnt vmcnt(0) lgkmcnt(0)
	s_barrier
	v_mov_b32_e32 v119, 1
	v_mov_b32_e32 v120, 0x9000
	v_mov_b32_e32 v121, 0x9280
	v_mov_b32_e32 v122, 0
	v_mov_b32_e32 v125, 0x10200
	s_mov_b32 s25, 0
	v_cmp_eq_u32_e32 vcc, 0, v0
	s_and_saveexec_b64 s[34:35], vcc
	s_cbranch_execz .Lcve_f0
	global_atomic_add v124, v121, v119, s[94:95] sc0
	s_waitcnt vmcnt(0)
	v_add_u32_e32 v124, 1, v124
	ds_write_b32 v125, v124 offset:4
.Lcve_f0:
	s_mov_b64 exec, s[34:35]
	s_waitcnt lgkmcnt(0)
	s_barrier
	ds_read_b32 v127, v125 offset:4
	s_waitcnt lgkmcnt(0)
	v_readfirstlane_b32 s25, v127
	s_cmpk_ge_u32 s25, 0x100
	s_cbranch_scc1 .Lcve_done
	s_barrier
	v_lshrrev_b32_e32 v104, 5, v0
	v_and_b32_e32 v126, 31, v0
	v_lshlrev_b32_e32 v105, 13, v104
	v_lshl_add_u32 v105, v126, 4, v105
	v_add_u32_e32 v106, 0x20000, v105
	v_add_u32_e32 v107, 0x40000, v105
	v_add_u32_e32 v108, 0x60000, v105
	v_add_u32_e32 v109, 0x80000, v105
	v_add_u32_e32 v110, 0xa0000, v105
	v_add_u32_e32 v111, 0xc0000, v105
	v_add_u32_e32 v112, 0xe0000, v105
	v_mul_u32_u24_e32 v113, 0x204, v104
	v_lshl_add_u32 v113, v126, 4, v113
	v_lshrrev_b32_e32 v127, 4, v0
	v_and_b32_e32 v126, 15, v0
	v_mul_u32_u24_e32 v114, 0x1020, v126
	v_lshl_add_u32 v114, v127, 2, v114
	v_lshlrev_b32_e32 v115, 12, v127
	v_lshl_add_u32 v115, v126, 4, v115
	v_add_u32_e32 v116, 0x20000, v115
	v_add_u32_e32 v117, 0x40000, v115
	v_add_u32_e32 v118, 0x60000, v115
	v_readlane_b32 s42, v254, 27
	v_readlane_b32 s43, v254, 28
	s_sub_u32 s42, s42, 0x28
	s_subb_u32 s43, s43, 0
	s_load_dwordx2 s[40:41], s[42:43], 0x0
	s_waitcnt lgkmcnt(0)
	v_cmp_eq_u32_e32 vcc, 0, v0
	s_and_saveexec_b64 s[34:35], vcc
	s_cbranch_execz .Lcve_t0a
	global_atomic_add v123, v120, v119, s[94:95] sc0
	s_waitcnt vmcnt(0)
	ds_write_b32 v125, v123
	ds_write_b32 v125, v122 offset:4

; __device__ __forceinline__ void lds_barrier() { asm volatile("s_waitcnt lgkmcnt(0)" ::: "memory"); __builtin_amdgcn_s_barrier(); asm volatile("" ::: "memory"); }
; __device__ __forceinline__ unsigned xb_add(unsigned* p, unsigned v) { return __hip_atomic_fetch_add(p, v, __ATOMIC_RELAXED, __HIP_MEMORY_SCOPE_AGENT); }
; __device__ __forceinline__ void phase_prologue(const Args& a, LAS unsigned char* lds) {
;     ...
;         ++it;
;         if (tid == 0) { qs[it & 1] = pend; pend = (int)xb_add(cq_head, 1u); }
;         lds_barrier();
.Lcve_loop:
	ds_read_b32 v126, v125
	ds_read_b32 v127, v125 offset:4
	s_waitcnt lgkmcnt(0)
	v_readfirstlane_b32 s24, v126
	v_readfirstlane_b32 s25, v127
	s_cmpk_gt_u32 s24, 0x1fff
	s_cbranch_scc1 .Lcve_done
	s_cmpk_ge_u32 s25, 0x100
	s_cbranch_scc1 .Lcve_nopf
	v_cmp_eq_u32_e32 vcc, 0, v0
	s_and_saveexec_b64 s[34:35], vcc
	s_cbranch_execz .Lcve_t0b
	global_atomic_add v123, v120, v119, s[94:95] sc0
	global_atomic_add v124, v121, v122, s[94:95] sc0

; #define LAS __attribute__((address_space(3)))
; __device__ __forceinline__ void xcd_barrier_complete(unsigned* bar, unsigned x, unsigned& nloc, unsigned& nx) {
;     const unsigned G = gridDim.x * gridDim.y * gridDim.z;
;     unsigned sum, cnt, mine, sp = 0u;
;     for (;;) {
;         sum = 0u; cnt = 0u; mine = 0u;
; #pragma unroll
;         for (unsigned j = 0; j < 16; ++j) { const unsigned c = xb_ld(&bar[XB_XCNT(j)]); sum += c; cnt += (c > 0u) ? 1u : 0u; mine = (j == x) ? c : mine; }
;         if (sum == G) break;
;         __builtin_amdgcn_s_sleep(1);
;         if ((++sp & 255u) == 0u) { if (xb_ld(&bar[XB_TMO])) break; if (sp > XB_SPIN_CAP) { atomicAdd(&bar[XB_TMO], 1u); break; } }
;     }
;     nloc = mine > 0u ? mine : 1u; nx = cnt > 0u ? cnt : 1u;
; }
; __device__ __forceinline__ void xcd_barrier(const XcdBarrier& b) {
;     asm volatile("s_waitcnt vmcnt(0)" ::: "memory");
;     __syncthreads();
;     if (threadIdx.x == 0) {
;         unsigned* bar = b.bar;
;         __builtin_amdgcn_s_waitcnt(0);
;         unsigned nloc = b.st[0], nx = b.st[1];
; __device__ __forceinline__ void phase_prologue(const Args& a, LAS unsigned char* lds) {
;     ...
;         const int kt = r / NT, ntl = r % NT, k0 = kt * 128, n0 = ntl * 128;
;         const int drow0 = mode == 0 ? n0 : (ntl * 256 + (mode == 2 ? 128 : 0));
;         f32x4 v[8];
; #pragma unroll
;         for (int i = 0; i < 8; ++i) { const int id = tid + 512 * i, row = id >> 5, c4 = id & 31, n = n0 + c4 * 4;
;             v[i] = (f32x4){0.f, 0.f, 0.f, 0.f};
;             if (n < nvalid) v[i] = *(const f32x4*)(src + (size_t)(k0 + row) * ldn + n); }
; #pragma unroll
;         for (int i = 0; i < 8; ++i) { const int id = tid + 512 * i, row = id >> 5, c4 = id & 31;
;             LAS float* tp = tile + row * 129 + c4 * 4; tp[0] = v[i][0]; tp[1] = v[i][1]; tp[2] = v[i][2]; tp[3] = v[i][3]; }
;         lds_barrier();
; #pragma unroll
;         for (int i = 0; i < 4; ++i) { const int piece = tid + 512 * i, nl = piece >> 4, kg = piece & 15; const LAS float* s = tile + (kg * 8) * 129 + nl;
;             u32x4 o; o.x = pk2(s[0], s[129]); o.y = pk2(s[258], s[387]); o.z = pk2(s[516], s[645]); o.w = pk2(s[774], s[903]);
;             *(u32x4*)(dst + (size_t)(drow0 + nl) * 2048 + k0 + kg * 8) = o; }
;         ++it;
;         if (tid == 0) { qs[it & 1] = pend; pend = (int)xb_add(cq_head, 1u); }
.Lcve_nopf:
	s_lshr_b32 s36, s24, 12
	s_bfe_u32 s30, s24, 0x40008
	s_add_i32 s30, s30, 16
	s_lshl_b32 s30, s30, 24
	s_bfe_u32 s31, s24, 0x40004
	s_and_b32 s32, s24, 15
	v_readlane_b32 s26, v254, 43
	v_readlane_b32 s27, v254, 44
	s_cmp_lg_u32 s36, 0
	s_cselect_b32 s26, s40, s26
	s_cselect_b32 s27, s41, s27
	s_lshl_b32 s33, s31, 20
	s_add_i32 s33, s33, s30
	s_lshl_b32 s37, s32, 9
	s_add_i32 s33, s33, s37
	s_add_u32 s26, s26, s33
	s_addc_u32 s27, s27, 0
	v_readlane_b32 s28, v254, 25
	v_readlane_b32 s29, v254, 26
	s_lshl_b32 s33, s32, 20
	s_add_i32 s33, s33, s30
	s_lshl_b32 s37, s36, 19
	s_add_i32 s33, s33, s37
	s_lshl_b32 s37, s31, 8
	s_add_i32 s33, s33, s37
	s_add_u32 s28, s28, s33
	s_addc_u32 s29, s29, 0
	global_load_dwordx4 v[128:131], v105, s[26:27]
	global_load_dwordx4 v[132:135], v106, s[26:27]
	global_load_dwordx4 v[136:139], v107, s[26:27]
	global_load_dwordx4 v[140:143], v108, s[26:27]
	global_load_dwordx4 v[144:147], v109, s[26:27]
	global_load_dwordx4 v[148:151], v110, s[26:27]
	global_load_dwordx4 v[152:155], v111, s[26:27]
	global_load_dwordx4 v[156:159], v112, s[26:27]
	s_waitcnt vmcnt(7)
	ds_write_b32 v113, v128
	ds_write_b32 v113, v129 offset:4
	ds_write_b32 v113, v130 offset:8
	ds_write_b32 v113, v131 offset:12
	s_waitcnt vmcnt(6)
	ds_write_b32 v113, v132 offset:8256
	ds_write_b32 v113, v133 offset:8260
	ds_write_b32 v113, v134 offset:8264
	ds_write_b32 v113, v135 offset:8268
	s_waitcnt vmcnt(5)
	ds_write_b32 v113, v136 offset:16512
	ds_write_b32 v113, v137 offset:16516
	ds_write_b32 v113, v138 offset:16520
	ds_write_b32 v113, v139 offset:16524
	s_waitcnt vmcnt(4)
	ds_write_b32 v113, v140 offset:24768
	ds_write_b32 v113, v141 offset:24772
	ds_write_b32 v113, v142 offset:24776
	ds_write_b32 v113, v143 offset:24780
	s_waitcnt vmcnt(3)
	ds_write_b32 v113, v144 offset:33024
	ds_write_b32 v113, v145 offset:33028
	ds_write_b32 v113, v146 offset:33032
	ds_write_b32 v113, v147 offset:33036
	s_waitcnt vmcnt(2)
	ds_write_b32 v113, v148 offset:41280
	ds_write_b32 v113, v149 offset:41284
	ds_write_b32 v113, v150 offset:41288
	ds_write_b32 v113, v151 offset:41292
	s_waitcnt vmcnt(1)
	ds_write_b32 v113, v152 offset:49536
	ds_write_b32 v113, v153 offset:49540
	ds_write_b32 v113, v154 offset:49544
	ds_write_b32 v113, v155 offset:49548
	s_waitcnt vmcnt(0)
	ds_write_b32 v113, v156 offset:57792
	ds_write_b32 v113, v157 offset:57796
	ds_write_b32 v113, v158 offset:57800
	ds_write_b32 v113, v159 offset:57804
	s_waitcnt lgkmcnt(0)
	s_barrier
	ds_read_b32 v160, v114
	ds_read_b32 v161, v114 offset:516
	ds_read_b32 v162, v114 offset:1032
	ds_read_b32 v163, v114 offset:1548
	ds_read_b32 v164, v114 offset:2064
	ds_read_b32 v165, v114 offset:2580
	ds_read_b32 v166, v114 offset:3096
	ds_read_b32 v167, v114 offset:3612
	s_waitcnt lgkmcnt(0)
	v_cvt_pk_bf16_f32 v168, v160, v161
	v_cvt_pk_bf16_f32 v169, v162, v163
	v_cvt_pk_bf16_f32 v170, v164, v165
	v_cvt_pk_bf16_f32 v171, v166, v167
	global_store_dwordx4 v115, v[168:171], s[28:29]
	ds_read_b32 v160, v114 offset:128
	ds_read_b32 v161, v114 offset:644
	ds_read_b32 v162, v114 offset:1160
	ds_read_b32 v163, v114 offset:1676
	ds_read_b32 v164, v114 offset:2192
	ds_read_b32 v165, v114 offset:2708
	ds_read_b32 v166, v114 offset:3224
	ds_read_b32 v167, v114 offset:3740
	s_waitcnt lgkmcnt(0)
	v_cvt_pk_bf16_f32 v172, v160, v161
	v_cvt_pk_bf16_f32 v173, v162, v163
	v_cvt_pk_bf16_f32 v174, v164, v165
	v_cvt_pk_bf16_f32 v175, v166, v167
	global_store_dwordx4 v116, v[172:175], s[28:29]
	ds_read_b32 v160, v114 offset:256
	ds_read_b32 v161, v114 offset:772
	ds_read_b32 v162, v114 offset:1288
	ds_read_b32 v163, v114 offset:1804
	ds_read_b32 v164, v114 offset:2320
	ds_read_b32 v165, v114 offset:2836
	ds_read_b32 v166, v114 offset:3352
	ds_read_b32 v167, v114 offset:3868
	s_waitcnt lgkmcnt(0)
	v_cvt_pk_bf16_f32 v168, v160, v161
	v_cvt_pk_bf16_f32 v169, v162, v163
	v_cvt_pk_bf16_f32 v170, v164, v165
	v_cvt_pk_bf16_f32 v171, v166, v167
	global_store_dwordx4 v117, v[168:171], s[28:29]
	ds_read_b32 v160, v114 offset:384
	ds_read_b32 v161, v114 offset:900
	ds_read_b32 v162, v114 offset:1416
	ds_read_b32 v163, v114 offset:1932
	ds_read_b32 v164, v114 offset:2448
	ds_read_b32 v165, v114 offset:2964
	ds_read_b32 v166, v114 offset:3480
	ds_read_b32 v167, v114 offset:3996
	s_waitcnt lgkmcnt(0)
	v_cvt_pk_bf16_f32 v172, v160, v161
	v_cvt_pk_bf16_f32 v173, v162, v163
	v_cvt_pk_bf16_f32 v174, v164, v165
	v_cvt_pk_bf16_f32 v175, v166, v167
	global_store_dwordx4 v118, v[172:175], s[28:29]
	s_cmpk_ge_u32 s25, 0x100
	s_cbranch_scc1 .Lcve_done
	v_cmp_eq_u32_e32 vcc, 0, v0
	s_and_saveexec_b64 s[34:35], vcc
	s_cbranch_execz .Lcve_t0c
	s_waitcnt vmcnt(0)
	ds_write_b32 v125, v123
	ds_write_b32 v125, v124 offset:4
.Lcve_t0c:
	s_mov_b64 exec, s[34:35]
	s_waitcnt lgkmcnt(0)
	s_barrier
	s_branch .Lcve_loop
.Lcve_done:
	v_readlane_b32 s0, v254, 0
	v_readlane_b32 s1, v254, 1
	s_cmp_gt_i32 s1, 13
	s_cselect_b64 s[0:1], -1, 0
	s_and_b64 s[2:3], s[8:9], s[0:1]
	s_andn2_b64 vcc, exec, s[2:3]
	s_cbranch_vccnz .LBB0_1129
	s_waitcnt vmcnt(0)
	v_cmp_eq_u32_e32 vcc, 0, v0
	s_waitcnt vmcnt(0) lgkmcnt(0)
	s_barrier
	s_and_saveexec_b64 s[2:3], vcc
	s_cbranch_execz .LBB0_1128
	s_add_i32 s4, 0, 0x23fc0
	v_mov_b32_e32 v1, s4
	s_waitcnt vmcnt(0) expcnt(0) lgkmcnt(0)
	ds_read_b32 v3, v1
	s_add_i32 s4, 0, 0x23fc4
	v_mov_b32_e32 v1, s4
	ds_read_b32 v1, v1
	s_waitcnt lgkmcnt(1)
	v_cmp_ne_u32_e32 vcc, 0, v3
	s_cbranch_vccnz .LBB0_1096
	v_readlane_b32 s4, v254, 27
	v_readlane_b32 s5, v254, 28
	s_load_dwordx2 s[8:9], s[4:5], 0x4
	s_add_u32 s4, s94, 0x4200
	s_addc_u32 s5, s95, 0
	s_add_u32 s6, s94, 0x4400
	s_addc_u32 s7, s95, 0
	v_readlane_b32 s10, v255, 9
	s_waitcnt lgkmcnt(0)
	s_mul_i32 s33, s8, s10
	s_add_u32 s8, s94, 0x4500
	s_mul_i32 s33, s33, s9
	s_addc_u32 s9, s95, 0
	s_add_u32 s10, s94, 0x4600
	s_addc_u32 s11, s95, 0
	s_add_u32 s12, s94, 0x4700
	s_addc_u32 s13, s95, 0
	s_add_u32 s14, s94, 0x4800
	s_addc_u32 s15, s95, 0
	s_add_u32 s16, s94, 0x4900
	s_addc_u32 s17, s95, 0
	s_add_u32 s18, s94, 0x4a00
	s_addc_u32 s19, s95, 0
	s_add_u32 s20, s94, 0x4b00
	s_addc_u32 s21, s95, 0
	s_add_u32 s22, s94, 0x4c00
	s_addc_u32 s23, s95, 0
	s_add_u32 s24, s94, 0x4d00
	s_addc_u32 s25, s95, 0
	s_add_u32 s26, s94, 0x4e00
	s_addc_u32 s27, s95, 0
	s_add_u32 s28, s94, 0x4f00
	s_addc_u32 s29, s95, 0
	s_add_u32 s30, s94, 0x5000
	s_addc_u32 s31, s95, 0
	s_add_u32 s34, s94, 0x5100
	s_addc_u32 s35, s95, 0
	s_add_u32 s36, s94, 0x5200
	s_addc_u32 s37, s95, 0
	s_add_u32 s38, s94, 0x5300
	s_addc_u32 s39, s95, 0
	s_mov_b32 s46, 1
	v_mov_b32_e32 v17, 0
	s_branch .LBB0_1084

; #define LAS __attribute__((address_space(3)))
; __device__ __forceinline__ void lds_barrier() { asm volatile("s_waitcnt lgkmcnt(0)" ::: "memory"); __builtin_amdgcn_s_barrier(); asm volatile("" ::: "memory"); }
; __device__ __forceinline__ unsigned xb_add(unsigned* p, unsigned v) { return __hip_atomic_fetch_add(p, v, __ATOMIC_RELAXED, __HIP_MEMORY_SCOPE_AGENT); }
; __device__ __forceinline__ void phase_prologue(const Args& a, LAS unsigned char* lds) {
;     ...
;     unsigned* cq_head = (unsigned*)(a.ws + WS_CTL) + 8192 + 768;
;     volatile LAS int* qs = (volatile LAS int*)(lds + 128 * 129 * 4);
;     int pend = 0, it = 0;
;     if (tid == 0) { qs[0] = (int)xb_add(cq_head, 1u); pend = (int)xb_add(cq_head, 1u); }
;     __syncthreads();
;     for (int u = qs[0]; u < CTOT; u = qs[it & 1]) {
;     ...
;         const int kt = r / NT, ntl = r % NT, k0 = kt * 128, n0 = ntl * 128;
;         const int drow0 = mode == 0 ? n0 : (ntl * 256 + (mode == 2 ? 128 : 0));
;         f32x4 v[8];
; #pragma unroll
;         for (int i = 0; i < 8; ++i) { const int id = tid + 512 * i, row = id >> 5, c4 = id & 31, n = n0 + c4 * 4;
;             v[i] = (f32x4){0.f, 0.f, 0.f, 0.f};
;             if (n < nvalid) v[i] = *(const f32x4*)(src + (size_t)(k0 + row) * ldn + n); }
; #pragma unroll
;         for (int i = 0; i < 8; ++i) { const int id = tid + 512 * i, row = id >> 5, c4 = id & 31;
;             LAS float* tp = tile + row * 129 + c4 * 4; tp[0] = v[i][0]; tp[1] = v[i][1]; tp[2] = v[i][2]; tp[3] = v[i][3]; }
;         lds_barrier();
; #pragma unroll
;         for (int i = 0; i < 4; ++i) { const int piece = tid + 512 * i, nl = piece >> 4, kg = piece & 15; const LAS float* s = tile + (kg * 8) * 129 + nl;
;             u32x4 o; o.x = pk2(s[0], s[129]); o.y = pk2(s[258], s[387]); o.z = pk2(s[516], s[645]); o.w = pk2(s[774], s[903]);
;             *(u32x4*)(dst + (size_t)(drow0 + nl) * 2048 + k0 + kg * 8) = o; }
.Lcva_entry:
	s_waitcnt vmcnt(0) lgkmcnt(0)
	s_barrier
	v_mov_b32_e32 v119, 1
	v_mov_b32_e32 v120, 0x9000
	v_mov_b32_e32 v121, 0x9100
	v_mov_b32_e32 v122, 0
	v_mov_b32_e32 v125, 0x10200
	s_mov_b32 s25, 0
	v_cmp_eq_u32_e32 vcc, 0, v0
	s_and_saveexec_b64 s[34:35], vcc
	s_cbranch_execz .Lcva_f0
	global_atomic_add v124, v121, v122, s[94:95] sc0
	s_waitcnt vmcnt(0)
	ds_write_b32 v125, v124 offset:4
.Lcva_f0:
	s_mov_b64 exec, s[34:35]
	s_waitcnt lgkmcnt(0)
	s_barrier
	ds_read_b32 v127, v125 offset:4
	s_waitcnt lgkmcnt(0)
	v_readfirstlane_b32 s25, v127
	s_cmpk_ge_u32 s25, 0x1
	s_cbranch_scc1 .Lcva_done
	s_barrier
	v_lshrrev_b32_e32 v104, 5, v0
	v_and_b32_e32 v126, 31, v0
	v_lshlrev_b32_e32 v105, 13, v104
	v_lshl_add_u32 v105, v126, 4, v105
	v_add_u32_e32 v106, 0x20000, v105
	v_add_u32_e32 v107, 0x40000, v105
	v_add_u32_e32 v108, 0x60000, v105
	v_add_u32_e32 v109, 0x80000, v105
	v_add_u32_e32 v110, 0xa0000, v105
	v_add_u32_e32 v111, 0xc0000, v105
	v_add_u32_e32 v112, 0xe0000, v105
	v_mul_u32_u24_e32 v113, 0x204, v104
	v_lshl_add_u32 v113, v126, 4, v113
	v_lshrrev_b32_e32 v127, 4, v0
	v_and_b32_e32 v126, 15, v0
	v_mul_u32_u24_e32 v114, 0x1020, v126
	v_lshl_add_u32 v114, v127, 2, v114
	v_lshlrev_b32_e32 v115, 12, v127
	v_lshl_add_u32 v115, v126, 4, v115
	v_add_u32_e32 v116, 0x20000, v115
	v_add_u32_e32 v117, 0x40000, v115
	v_add_u32_e32 v118, 0x60000, v115
	v_readlane_b32 s42, v254, 27
	v_readlane_b32 s43, v254, 28
	s_sub_u32 s42, s42, 0x28
	s_subb_u32 s43, s43, 0
	s_load_dwordx2 s[40:41], s[42:43], 0x0
	s_waitcnt lgkmcnt(0)
	v_cmp_eq_u32_e32 vcc, 0, v0
	s_and_saveexec_b64 s[34:35], vcc
	s_cbranch_execz .Lcva_t0a
	global_atomic_add v123, v120, v119, s[94:95] sc0
	s_waitcnt vmcnt(0)
	ds_write_b32 v125, v123
	ds_write_b32 v125, v122 offset:4

; __device__ __forceinline__ void lds_barrier() { asm volatile("s_waitcnt lgkmcnt(0)" ::: "memory"); __builtin_amdgcn_s_barrier(); asm volatile("" ::: "memory"); }
; __device__ __forceinline__ unsigned xb_add(unsigned* p, unsigned v) { return __hip_atomic_fetch_add(p, v, __ATOMIC_RELAXED, __HIP_MEMORY_SCOPE_AGENT); }
; __device__ __forceinline__ void phase_prologue(const Args& a, LAS unsigned char* lds) {
;     ...
;         ++it;
;         if (tid == 0) { qs[it & 1] = pend; pend = (int)xb_add(cq_head, 1u); }
;         lds_barrier();
.Lcva_loop:
	ds_read_b32 v126, v125
	ds_read_b32 v127, v125 offset:4
	s_waitcnt lgkmcnt(0)
	v_readfirstlane_b32 s24, v126
	v_readfirstlane_b32 s25, v127
	s_cmpk_gt_u32 s24, 0x1fff
	s_cbranch_scc1 .Lcva_done
	s_cmpk_ge_u32 s25, 0x1
	s_cbranch_scc1 .Lcva_nopf
	v_cmp_eq_u32_e32 vcc, 0, v0
	s_and_saveexec_b64 s[34:35], vcc
	s_cbranch_execz .Lcva_t0b
	global_atomic_add v123, v120, v119, s[94:95] sc0
	global_atomic_add v124, v121, v122, s[94:95] sc0

; #define LAS __attribute__((address_space(3)))
; __device__ __forceinline__ void lds_barrier() { asm volatile("s_waitcnt lgkmcnt(0)" ::: "memory"); __builtin_amdgcn_s_barrier(); asm volatile("" ::: "memory"); }
; __device__ __forceinline__ unsigned xb_add(unsigned* p, unsigned v) { return __hip_atomic_fetch_add(p, v, __ATOMIC_RELAXED, __HIP_MEMORY_SCOPE_AGENT); }
; __device__ __forceinline__ void phase_prologue(const Args& a, LAS unsigned char* lds) {
;     ...
;         const int kt = r / NT, ntl = r % NT, k0 = kt * 128, n0 = ntl * 128;
;         const int drow0 = mode == 0 ? n0 : (ntl * 256 + (mode == 2 ? 128 : 0));
;         f32x4 v[8];
; #pragma unroll
;         for (int i = 0; i < 8; ++i) { const int id = tid + 512 * i, row = id >> 5, c4 = id & 31, n = n0 + c4 * 4;
;             v[i] = (f32x4){0.f, 0.f, 0.f, 0.f};
;             if (n < nvalid) v[i] = *(const f32x4*)(src + (size_t)(k0 + row) * ldn + n); }
; #pragma unroll
;         for (int i = 0; i < 8; ++i) { const int id = tid + 512 * i, row = id >> 5, c4 = id & 31;
;             LAS float* tp = tile + row * 129 + c4 * 4; tp[0] = v[i][0]; tp[1] = v[i][1]; tp[2] = v[i][2]; tp[3] = v[i][3]; }
;         lds_barrier();
; #pragma unroll
;         for (int i = 0; i < 4; ++i) { const int piece = tid + 512 * i, nl = piece >> 4, kg = piece & 15; const LAS float* s = tile + (kg * 8) * 129 + nl;
;             u32x4 o; o.x = pk2(s[0], s[129]); o.y = pk2(s[258], s[387]); o.z = pk2(s[516], s[645]); o.w = pk2(s[774], s[903]);
;             *(u32x4*)(dst + (size_t)(drow0 + nl) * 2048 + k0 + kg * 8) = o; }
;         ++it;
;         if (tid == 0) { qs[it & 1] = pend; pend = (int)xb_add(cq_head, 1u); }
;         lds_barrier();
.Lcva_nopf:
	s_lshr_b32 s36, s24, 12
	s_bfe_u32 s30, s24, 0x40008
	s_add_i32 s30, s30, 16
	s_lshl_b32 s30, s30, 24
	s_bfe_u32 s31, s24, 0x40004
	s_and_b32 s32, s24, 15
	v_readlane_b32 s26, v254, 43
	v_readlane_b32 s27, v254, 44
	s_cmp_lg_u32 s36, 0
	s_cselect_b32 s26, s40, s26
	s_cselect_b32 s27, s41, s27
	s_lshl_b32 s33, s31, 20
	s_add_i32 s33, s33, s30
	s_lshl_b32 s37, s32, 9
	s_add_i32 s33, s33, s37
	s_add_u32 s26, s26, s33
	s_addc_u32 s27, s27, 0
	v_readlane_b32 s28, v254, 25
	v_readlane_b32 s29, v254, 26
	s_lshl_b32 s33, s32, 20
	s_add_i32 s33, s33, s30
	s_lshl_b32 s37, s36, 19
	s_add_i32 s33, s33, s37
	s_lshl_b32 s37, s31, 8
	s_add_i32 s33, s33, s37
	s_add_u32 s28, s28, s33
	s_addc_u32 s29, s29, 0
	global_load_dwordx4 v[128:131], v105, s[26:27]
	global_load_dwordx4 v[132:135], v106, s[26:27]
	global_load_dwordx4 v[136:139], v107, s[26:27]
	global_load_dwordx4 v[140:143], v108, s[26:27]
	global_load_dwordx4 v[144:147], v109, s[26:27]
	global_load_dwordx4 v[148:151], v110, s[26:27]
	global_load_dwordx4 v[152:155], v111, s[26:27]
	global_load_dwordx4 v[156:159], v112, s[26:27]
	s_waitcnt vmcnt(7)
	ds_write_b32 v113, v128
	ds_write_b32 v113, v129 offset:4
	ds_write_b32 v113, v130 offset:8
	ds_write_b32 v113, v131 offset:12
	s_waitcnt vmcnt(6)
	ds_write_b32 v113, v132 offset:8256
	ds_write_b32 v113, v133 offset:8260
	ds_write_b32 v113, v134 offset:8264
	ds_write_b32 v113, v135 offset:8268
	s_waitcnt vmcnt(5)
	ds_write_b32 v113, v136 offset:16512
	ds_write_b32 v113, v137 offset:16516
	ds_write_b32 v113, v138 offset:16520
	ds_write_b32 v113, v139 offset:16524
	s_waitcnt vmcnt(4)
	ds_write_b32 v113, v140 offset:24768
	ds_write_b32 v113, v141 offset:24772
	ds_write_b32 v113, v142 offset:24776
	ds_write_b32 v113, v143 offset:24780
	s_waitcnt vmcnt(3)
	ds_write_b32 v113, v144 offset:33024
	ds_write_b32 v113, v145 offset:33028
	ds_write_b32 v113, v146 offset:33032
	ds_write_b32 v113, v147 offset:33036
	s_waitcnt vmcnt(2)
	ds_write_b32 v113, v148 offset:41280
	ds_write_b32 v113, v149 offset:41284
	ds_write_b32 v113, v150 offset:41288
	ds_write_b32 v113, v151 offset:41292
	s_waitcnt vmcnt(1)
	ds_write_b32 v113, v152 offset:49536
	ds_write_b32 v113, v153 offset:49540
	ds_write_b32 v113, v154 offset:49544
	ds_write_b32 v113, v155 offset:49548
	s_waitcnt vmcnt(0)
	ds_write_b32 v113, v156 offset:57792
	ds_write_b32 v113, v157 offset:57796
	ds_write_b32 v113, v158 offset:57800
	ds_write_b32 v113, v159 offset:57804
	s_waitcnt lgkmcnt(0)
	s_barrier
	ds_read_b32 v160, v114
	ds_read_b32 v161, v114 offset:516
	ds_read_b32 v162, v114 offset:1032
	ds_read_b32 v163, v114 offset:1548
	ds_read_b32 v164, v114 offset:2064
	ds_read_b32 v165, v114 offset:2580
	ds_read_b32 v166, v114 offset:3096
	ds_read_b32 v167, v114 offset:3612
	s_waitcnt lgkmcnt(0)
	v_cvt_pk_bf16_f32 v168, v160, v161
	v_cvt_pk_bf16_f32 v169, v162, v163
	v_cvt_pk_bf16_f32 v170, v164, v165
	v_cvt_pk_bf16_f32 v171, v166, v167
	global_store_dwordx4 v115, v[168:171], s[28:29]
	ds_read_b32 v160, v114 offset:128
	ds_read_b32 v161, v114 offset:644
	ds_read_b32 v162, v114 offset:1160
	ds_read_b32 v163, v114 offset:1676
	ds_read_b32 v164, v114 offset:2192
	ds_read_b32 v165, v114 offset:2708
	ds_read_b32 v166, v114 offset:3224
	ds_read_b32 v167, v114 offset:3740
	s_waitcnt lgkmcnt(0)
	v_cvt_pk_bf16_f32 v172, v160, v161
	v_cvt_pk_bf16_f32 v173, v162, v163
	v_cvt_pk_bf16_f32 v174, v164, v165
	v_cvt_pk_bf16_f32 v175, v166, v167
	global_store_dwordx4 v116, v[172:175], s[28:29]
	ds_read_b32 v160, v114 offset:256
	ds_read_b32 v161, v114 offset:772
	ds_read_b32 v162, v114 offset:1288
	ds_read_b32 v163, v114 offset:1804
	ds_read_b32 v164, v114 offset:2320
	ds_read_b32 v165, v114 offset:2836
	ds_read_b32 v166, v114 offset:3352
	ds_read_b32 v167, v114 offset:3868
	s_waitcnt lgkmcnt(0)
	v_cvt_pk_bf16_f32 v168, v160, v161
	v_cvt_pk_bf16_f32 v169, v162, v163
	v_cvt_pk_bf16_f32 v170, v164, v165
	v_cvt_pk_bf16_f32 v171, v166, v167
	global_store_dwordx4 v117, v[168:171], s[28:29]
	ds_read_b32 v160, v114 offset:384
	ds_read_b32 v161, v114 offset:900
	ds_read_b32 v162, v114 offset:1416
	ds_read_b32 v163, v114 offset:1932
	ds_read_b32 v164, v114 offset:2448
	ds_read_b32 v165, v114 offset:2964
	ds_read_b32 v166, v114 offset:3480
	ds_read_b32 v167, v114 offset:3996
	s_waitcnt lgkmcnt(0)
	v_cvt_pk_bf16_f32 v172, v160, v161
	v_cvt_pk_bf16_f32 v173, v162, v163
	v_cvt_pk_bf16_f32 v174, v164, v165
	v_cvt_pk_bf16_f32 v175, v166, v167
	global_store_dwordx4 v118, v[172:175], s[28:29]
	s_cmpk_ge_u32 s25, 0x1
	s_cbranch_scc1 .Lcva_done
	v_cmp_eq_u32_e32 vcc, 0, v0
	s_and_saveexec_b64 s[34:35], vcc
	s_cbranch_execz .Lcva_t0c
	s_waitcnt vmcnt(0)
	ds_write_b32 v125, v123
	ds_write_b32 v125, v124 offset:4

; #define LAS __attribute__((address_space(3)))
; __device__ __forceinline__ unsigned xb_add(unsigned* p, unsigned v) { return __hip_atomic_fetch_add(p, v, __ATOMIC_RELAXED, __HIP_MEMORY_SCOPE_AGENT); }
; __device__ __forceinline__ void phase_prologue(const Args& a, LAS unsigned char* lds) {
;     ...
;     unsigned* cq_head = (unsigned*)(a.ws + WS_CTL) + 8192 + 768;
;     volatile LAS int* qs = (volatile LAS int*)(lds + 128 * 129 * 4);
;     int pend = 0, it = 0;
;     if (tid == 0) { qs[0] = (int)xb_add(cq_head, 1u); pend = (int)xb_add(cq_head, 1u); }
;     __syncthreads();
.LBB0_1442:
.Lcvb_entry:
	s_waitcnt vmcnt(0) lgkmcnt(0)
	s_barrier
	v_mov_b32_e32 v119, 1
	v_mov_b32_e32 v120, 0x9000
	v_mov_b32_e32 v121, 0x9300
	v_mov_b32_e32 v122, 0
	v_mov_b32_e32 v125, 0x10200
	s_mov_b32 s25, 0
	v_cmp_eq_u32_e32 vcc, 0, v0
	s_and_saveexec_b64 s[34:35], vcc
	s_cbranch_execz .Lcvb_f0
	global_atomic_add v124, v121, v119, s[94:95] sc0
	s_waitcnt vmcnt(0)
	v_add_u32_e32 v124, 1, v124
	ds_write_b32 v125, v124 offset:4

; #define LAS __attribute__((address_space(3)))
; __device__ __forceinline__ void phase_prologue(const Args& a, LAS unsigned char* lds) {
;     ...
;     unsigned* cq_head = (unsigned*)(a.ws + WS_CTL) + 8192 + 768;
;     volatile LAS int* qs = (volatile LAS int*)(lds + 128 * 129 * 4);
;     int pend = 0, it = 0;
;     if (tid == 0) { qs[0] = (int)xb_add(cq_head, 1u); pend = (int)xb_add(cq_head, 1u); }
;     __syncthreads();
;     for (int u = qs[0]; u < CTOT; u = qs[it & 1]) {
;         int r = u; const float* src; int ldn, nvalid, NT, mode = 0; bf16_t* dst;
;         if (r < CJ0) { src = a.in[I_EVIN]; ldn = 6144; nvalid = 6144; NT = 48; dst = (bf16_t*)(a.ws + WS_WIN0); }
;         else if ((r -= CJ0) < CJ1) { src = a.in[I_EVOUT]; ldn = 2048; nvalid = 2048; NT = 16; dst = (bf16_t*)(a.ws + WS_WOUT0); }
;         else if ((r -= CJ1) < CJ2) { src = a.in[I_ODIN]; ldn = 6176; nvalid = 6176; NT = 50; dst = (bf16_t*)(a.ws + WS_WIN1); }
;         else if ((r -= CJ2) < CJ3) { src = a.in[I_ODOUT]; ldn = 2048; nvalid = 2048; NT = 16; dst = (bf16_t*)(a.ws + WS_WOUT1); }
;         else { r -= CJ3; const int which = r / CJM; r -= which * CJM; const int mtx = r >> 8; r &= 255; ldn = 2048; nvalid = 2048; NT = 16;
;             if (which == 0) { src = a.in[I_WGATE] + (size_t)mtx * 2048 * 2048; dst = (bf16_t*)(a.ws + WS_WGU) + (size_t)mtx * 4096 * 2048; mode = 1; }
;             else if (which == 1) { src = a.in[I_WUP] + (size_t)mtx * 2048 * 2048; dst = (bf16_t*)(a.ws + WS_WGU) + (size_t)mtx * 4096 * 2048; mode = 2; }
;             else { src = a.in[I_WDOWN] + (size_t)mtx * 2048 * 2048; dst = (bf16_t*)(a.ws + WS_WDN) + (size_t)mtx * 2048 * 2048; } }
;         const int kt = r / NT, ntl = r % NT, k0 = kt * 128, n0 = ntl * 128;
;         const int drow0 = mode == 0 ? n0 : (ntl * 256 + (mode == 2 ? 128 : 0));
;         f32x4 v[8];
; #pragma unroll
;         for (int i = 0; i < 8; ++i) { const int id = tid + 512 * i, row = id >> 5, c4 = id & 31, n = n0 + c4 * 4;
;             v[i] = (f32x4){0.f, 0.f, 0.f, 0.f};
;             if (n < nvalid) v[i] = *(const f32x4*)(src + (size_t)(k0 + row) * ldn + n); }
; #pragma unroll
;         for (int i = 0; i < 8; ++i) { const int id = tid + 512 * i, row = id >> 5, c4 = id & 31;
;             LAS float* tp = tile + row * 129 + c4 * 4; tp[0] = v[i][0]; tp[1] = v[i][1]; tp[2] = v[i][2]; tp[3] = v[i][3]; }
;         lds_barrier();
; #pragma unroll
.LBB0_1648:
.Lcvz_entry:
	s_waitcnt vmcnt(0) lgkmcnt(0)
	s_barrier
	v_mov_b32_e32 v119, 1
	v_mov_b32_e32 v120, 0x9000
	v_mov_b32_e32 v122, 0
	v_mov_b32_e32 v125, 0x10200
	s_mov_b32 s25, 0
	v_lshrrev_b32_e32 v104, 5, v0
	v_and_b32_e32 v126, 31, v0
	v_lshlrev_b32_e32 v105, 13, v104
	v_lshl_add_u32 v105, v126, 4, v105
	v_add_u32_e32 v106, 0x20000, v105
	v_add_u32_e32 v107, 0x40000, v105
	v_add_u32_e32 v108, 0x60000, v105
	v_add_u32_e32 v109, 0x80000, v105
	v_add_u32_e32 v110, 0xa0000, v105
	v_add_u32_e32 v111, 0xc0000, v105
	v_add_u32_e32 v112, 0xe0000, v105
	v_mul_u32_u24_e32 v113, 0x204, v104
	v_lshl_add_u32 v113, v126, 4, v113
	v_lshrrev_b32_e32 v127, 4, v0
	v_and_b32_e32 v126, 15, v0
	v_mul_u32_u24_e32 v114, 0x1020, v126
	v_lshl_add_u32 v114, v127, 2, v114
	v_lshlrev_b32_e32 v115, 12, v127
	v_lshl_add_u32 v115, v126, 4, v115
	v_add_u32_e32 v116, 0x20000, v115
	v_add_u32_e32 v117, 0x40000, v115
	v_add_u32_e32 v118, 0x60000, v115
	v_readlane_b32 s42, v254, 27
	v_readlane_b32 s43, v254, 28
	s_sub_u32 s42, s42, 0x28
	s_subb_u32 s43, s43, 0
	s_load_dwordx2 s[40:41], s[42:43], 0x0
	s_waitcnt lgkmcnt(0)
	v_cmp_eq_u32_e32 vcc, 0, v0
	s_and_saveexec_b64 s[34:35], vcc
	s_cbranch_execz .Lcvz_t0a
	global_atomic_add v123, v120, v119, s[94:95] sc0
	s_waitcnt vmcnt(0)
	ds_write_b32 v125, v123

; __device__ __forceinline__ unsigned xb_ld(unsigned* p)              { return __hip_atomic_load(p, __ATOMIC_RELAXED, __HIP_MEMORY_SCOPE_AGENT); }
; __device__ __forceinline__ void xcd_barrier_complete(unsigned* bar, unsigned x, unsigned& nloc, unsigned& nx) {
;     const unsigned G = gridDim.x * gridDim.y * gridDim.z;
;     unsigned sum, cnt, mine, sp = 0u;
;     for (;;) {
;         sum = 0u; cnt = 0u; mine = 0u;
; #pragma unroll
;         for (unsigned j = 0; j < 16; ++j) { const unsigned c = xb_ld(&bar[XB_XCNT(j)]); sum += c; cnt += (c > 0u) ? 1u : 0u; mine = (j == x) ? c : mine; }
;         if (sum == G) break;
;         __builtin_amdgcn_s_sleep(1);
;         if ((++sp & 255u) == 0u) { if (xb_ld(&bar[XB_TMO])) break; if (sp > XB_SPIN_CAP) { atomicAdd(&bar[XB_TMO], 1u); break; } }
;     }
;     nloc = mine > 0u ? mine : 1u; nx = cnt > 0u ? cnt : 1u;
; }
; __device__ __forceinline__ void xcd_barrier(const XcdBarrier& b) {
;     asm volatile("s_waitcnt vmcnt(0)" ::: "memory");
;     __syncthreads();
;     if (threadIdx.x == 0) {
;         unsigned* bar = b.bar;
;         __builtin_amdgcn_s_waitcnt(0);
;         unsigned nloc = b.st[0], nx = b.st[1];
;         if (nloc == 0u) { xcd_barrier_complete(bar, b.x, nloc, nx); b.st[0] = nloc; b.st[1] = nx; }
.Lcvz_t0c:
	s_mov_b64 exec, s[34:35]
	s_waitcnt lgkmcnt(0)
	s_barrier
	s_branch .Lcvz_loop
.Lcvz_done:
	v_readlane_b32 s0, v254, 0
	v_readlane_b32 s1, v254, 1
	s_cmp_gt_i32 s1, 19
	s_cselect_b64 s[0:1], -1, 0
	s_and_b64 s[2:3], s[2:3], s[0:1]
	s_andn2_b64 vcc, exec, s[2:3]
	s_cbranch_vccnz .LBB0_1698
	s_waitcnt vmcnt(0)
	v_cmp_eq_u32_e32 vcc, 0, v0
	s_waitcnt vmcnt(0) lgkmcnt(0)
	s_barrier
	s_and_saveexec_b64 s[2:3], vcc
	s_cbranch_execz .LBB0_1697
	s_add_i32 s4, 0, 0x23fc0
	v_mov_b32_e32 v1, s4
	s_waitcnt vmcnt(0) expcnt(0) lgkmcnt(0)
	ds_read_b32 v3, v1
	s_add_i32 s4, 0, 0x23fc4
	v_mov_b32_e32 v1, s4
	ds_read_b32 v1, v1
	s_waitcnt lgkmcnt(1)
	v_cmp_ne_u32_e32 vcc, 0, v3
	s_cbranch_vccnz .LBB0_1665
	v_readlane_b32 s4, v254, 27
	v_readlane_b32 s5, v254, 28
	s_load_dwordx2 s[8:9], s[4:5], 0x4
	s_add_u32 s4, s94, 0x4200
	s_addc_u32 s5, s95, 0
	s_add_u32 s6, s94, 0x4400
	s_addc_u32 s7, s95, 0
	v_readlane_b32 s10, v255, 9
	s_waitcnt lgkmcnt(0)
	s_mul_i32 s33, s8, s10
	s_add_u32 s8, s94, 0x4500
	s_mul_i32 s33, s33, s9
	s_addc_u32 s9, s95, 0
	s_add_u32 s10, s94, 0x4600
	s_addc_u32 s11, s95, 0
	s_add_u32 s12, s94, 0x4700
	s_addc_u32 s13, s95, 0
	s_add_u32 s14, s94, 0x4800
	s_addc_u32 s15, s95, 0
	s_add_u32 s16, s94, 0x4900
	s_addc_u32 s17, s95, 0
	s_add_u32 s18, s94, 0x4a00
	s_addc_u32 s19, s95, 0
	s_add_u32 s20, s94, 0x4b00
	s_addc_u32 s21, s95, 0
	s_add_u32 s22, s94, 0x4c00
	s_addc_u32 s23, s95, 0
	s_add_u32 s24, s94, 0x4d00
	s_addc_u32 s25, s95, 0
	s_add_u32 s26, s94, 0x4e00
	s_addc_u32 s27, s95, 0
	s_add_u32 s28, s94, 0x4f00
	s_addc_u32 s29, s95, 0
	s_add_u32 s30, s94, 0x5000
	s_addc_u32 s31, s95, 0
	s_add_u32 s34, s94, 0x5100
	s_addc_u32 s35, s95, 0
	s_add_u32 s36, s94, 0x5200
	s_addc_u32 s37, s95, 0
	s_add_u32 s38, s94, 0x5300
	s_addc_u32 s39, s95, 0
	s_mov_b32 s46, 1
	v_mov_b32_e32 v17, 0
	s_branch .LBB0_1653
